# stack12: stack9 plus final-phase RMS all-reduce via DPP and final combine loop without the per-token store drain
# baseline (speedup 1.0000x reference)
; __device__ __forceinline__ float bflo(unsigned x) { return __uint_as_float(x << 16); }
; __device__ __forceinline__ float bfhi(unsigned x) { return __uint_as_float(x & 0xffff0000u); }
; __device__ __forceinline__ void phase_final(const bf16_t* XA, const bf16_t* Y, const int* tok_info, const float* g, float* out, int wid, int lane) {
;     ...
;         f32x4 v[8]; float ss = 0.f;
; #pragma unroll
;         for (int j = 0; j < 8; ++j) { const u32x2 xw = xr[j], a = ya[j], b = yb[j]; f32x4 xv = (f32x4){bflo(xw.x), bfhi(xw.x), bflo(xw.y), bfhi(xw.y)};
;             xv[0] += bflo(a.x) + bflo(b.x); xv[1] += bfhi(a.x) + bfhi(b.x); xv[2] += bflo(a.y) + bflo(b.y); xv[3] += bfhi(a.y) + bfhi(b.y);
;             v[j] = xv; ss += (xv[0] * xv[0] + xv[1] * xv[1]) + (xv[2] * xv[2] + xv[3] * xv[3]); }
.LBB0_2983:
	v_lshlrev_b32_e32 v146, 16, v138
	v_and_b32_e32 v147, 0xffff0000, v138
	v_lshlrev_b32_e32 v148, 16, v126
	v_and_b32_e32 v149, 0xffff0000, v126
	v_lshlrev_b32_e32 v120, 16, v124
	v_and_b32_e32 v121, 0xffff0000, v124
	v_pk_add_f32 v[146:147], v[148:149], v[146:147]
	v_lshlrev_b32_e32 v138, 16, v139
	v_and_b32_e32 v139, 0xffff0000, v139
	v_lshlrev_b32_e32 v126, 16, v127
	v_and_b32_e32 v127, 0xffff0000, v127
	v_pk_add_f32 v[120:121], v[146:147], v[120:121]
	v_lshlrev_b32_e32 v124, 16, v125
	v_and_b32_e32 v125, 0xffff0000, v125
	v_pk_add_f32 v[126:127], v[126:127], v[138:139]
	v_lshlrev_b32_e32 v138, 16, v136
	v_and_b32_e32 v139, 0xffff0000, v136
	v_lshlrev_b32_e32 v146, 16, v134
	v_and_b32_e32 v147, 0xffff0000, v134
	v_pk_add_f32 v[124:125], v[126:127], v[124:125]
	v_lshlrev_b32_e32 v126, 16, v132
	v_and_b32_e32 v127, 0xffff0000, v132
	v_pk_add_f32 v[138:139], v[146:147], v[138:139]
	v_lshlrev_b32_e32 v136, 16, v137
	v_and_b32_e32 v137, 0xffff0000, v137
	v_lshlrev_b32_e32 v134, 16, v135
	v_and_b32_e32 v135, 0xffff0000, v135
	v_pk_add_f32 v[126:127], v[138:139], v[126:127]
	v_lshlrev_b32_e32 v132, 16, v133
	v_and_b32_e32 v133, 0xffff0000, v133
	v_pk_add_f32 v[134:135], v[134:135], v[136:137]
	v_mov_b32_e32 v136, v121
	v_pk_add_f32 v[132:133], v[134:135], v[132:133]
	v_mov_b32_e32 v137, v127
	v_mov_b32_e32 v134, v120
	v_mov_b32_e32 v135, v126
	v_pk_mul_f32 v[136:137], v[136:137], v[136:137]
	v_mov_b32_e32 v138, v125
	v_mov_b32_e32 v139, v133
	v_pk_fma_f32 v[134:135], v[134:135], v[134:135], v[136:137]
	v_mov_b32_e32 v136, v124
	v_mov_b32_e32 v137, v132
	v_pk_mul_f32 v[138:139], v[138:139], v[138:139]
	v_lshlrev_b32_e32 v146, 16, v128
	v_pk_fma_f32 v[136:137], v[136:137], v[136:137], v[138:139]
	v_lshlrev_b32_e32 v138, 16, v130
	v_pk_add_f32 v[134:135], v[134:135], v[136:137]
	v_and_b32_e32 v139, 0xffff0000, v130
	v_and_b32_e32 v147, 0xffff0000, v128
	v_lshlrev_b32_e32 v130, 16, v131
	v_and_b32_e32 v131, 0xffff0000, v131
	v_lshlrev_b32_e32 v128, 16, v129
	v_and_b32_e32 v129, 0xffff0000, v129
	v_pk_add_f32 v[136:137], v[134:135], v[134:135] op_sel:[0,1] op_sel_hi:[1,0]
	v_lshlrev_b32_e32 v134, 16, v122
	v_and_b32_e32 v135, 0xffff0000, v122
	v_pk_add_f32 v[138:139], v[146:147], v[138:139]
	v_lshlrev_b32_e32 v122, 16, v123
	v_and_b32_e32 v123, 0xffff0000, v123
	v_pk_add_f32 v[128:129], v[128:129], v[130:131]
	v_pk_add_f32 v[134:135], v[138:139], v[134:135]
	v_pk_add_f32 v[122:123], v[128:129], v[122:123]
	v_mov_b32_e32 v130, v135
	v_mov_b32_e32 v131, v123
	v_mov_b32_e32 v128, v134
	v_mov_b32_e32 v129, v122
	v_pk_mul_f32 v[130:131], v[130:131], v[130:131]
	v_lshlrev_b32_e32 v138, 16, v118
	v_pk_fma_f32 v[128:129], v[128:129], v[128:129], v[130:131]
	v_and_b32_e32 v139, 0xffff0000, v118
	v_lshlrev_b32_e32 v146, 16, v116
	v_and_b32_e32 v147, 0xffff0000, v116
	v_pk_add_f32 v[130:131], v[128:129], v[128:129] op_sel:[0,1] op_sel_hi:[1,0]
	v_lshlrev_b32_e32 v128, 16, v114
	v_and_b32_e32 v129, 0xffff0000, v114
	v_pk_add_f32 v[138:139], v[146:147], v[138:139]
	v_lshlrev_b32_e32 v118, 16, v119
	v_and_b32_e32 v119, 0xffff0000, v119
	v_lshlrev_b32_e32 v116, 16, v117
	v_and_b32_e32 v117, 0xffff0000, v117
	v_pk_add_f32 v[128:129], v[138:139], v[128:129]
	v_lshlrev_b32_e32 v114, 16, v115
	v_and_b32_e32 v115, 0xffff0000, v115
	v_pk_add_f32 v[116:117], v[116:117], v[118:119]
	v_lshlrev_b32_e32 v146, 16, v112
	v_and_b32_e32 v147, 0xffff0000, v112
	v_lshlrev_b32_e32 v148, 16, v110
	v_and_b32_e32 v149, 0xffff0000, v110
	v_lshlrev_b32_e32 v112, 16, v113
	v_and_b32_e32 v113, 0xffff0000, v113
	v_lshlrev_b32_e32 v110, 16, v111
	v_and_b32_e32 v111, 0xffff0000, v111
	v_pk_add_f32 v[114:115], v[116:117], v[114:115]
	v_mul_f32_e32 v2, v129, v129
	v_lshlrev_b32_e32 v138, 16, v108
	v_and_b32_e32 v139, 0xffff0000, v108
	v_pk_add_f32 v[146:147], v[148:149], v[146:147]
	v_lshlrev_b32_e32 v108, 16, v109
	v_and_b32_e32 v109, 0xffff0000, v109
	v_pk_add_f32 v[110:111], v[110:111], v[112:113]
	v_pk_fma_f32 v[116:117], v[128:129], v[128:129], v[2:3] op_sel_hi:[1,1,0]
	v_mul_f32_e32 v2, v115, v115
	v_pk_add_f32 v[138:139], v[146:147], v[138:139]
	v_pk_add_f32 v[108:109], v[110:111], v[108:109]
	v_pk_fma_f32 v[118:119], v[114:115], v[114:115], v[2:3] op_sel_hi:[1,1,0]
	v_pk_mul_f32 v[110:111], v[138:139], v[138:139]
	v_pk_mul_f32 v[112:113], v[108:109], v[108:109]
	v_mov_b32_e32 v137, v110
	v_mov_b32_e32 v131, v111
	v_mov_b32_e32 v117, v112
	v_mov_b32_e32 v119, v113
	v_pk_add_f32 v[110:111], v[136:137], v[130:131]
	v_pk_add_f32 v[112:113], v[116:117], v[118:119]
	v_lshlrev_b32_e32 v116, 16, v106
	v_and_b32_e32 v117, 0xffff0000, v106
	v_lshlrev_b32_e32 v118, 16, v104
	v_and_b32_e32 v119, 0xffff0000, v104
	v_lshlrev_b32_e32 v106, 16, v107
	v_and_b32_e32 v107, 0xffff0000, v107
	v_lshlrev_b32_e32 v104, 16, v105
	v_and_b32_e32 v105, 0xffff0000, v105
	v_pk_add_f32 v[110:111], v[110:111], v[112:113]
	v_lshlrev_b32_e32 v112, 16, v102
	v_and_b32_e32 v113, 0xffff0000, v102
	v_pk_add_f32 v[116:117], v[118:119], v[116:117]
	v_lshlrev_b32_e32 v102, 16, v103
	v_and_b32_e32 v103, 0xffff0000, v103
	v_pk_add_f32 v[104:105], v[104:105], v[106:107]
	v_pk_add_f32 v[112:113], v[116:117], v[112:113]
	v_pk_add_f32 v[104:105], v[104:105], v[102:103]
	v_mov_b32_e32 v106, v113
	v_mov_b32_e32 v107, v105
	v_mov_b32_e32 v102, v112
	v_mov_b32_e32 v103, v104
	v_pk_mul_f32 v[106:107], v[106:107], v[106:107]
	v_lshlrev_b32_e32 v116, 16, v100
	v_and_b32_e32 v117, 0xffff0000, v100
	v_lshlrev_b32_e32 v118, 16, v96
	v_and_b32_e32 v119, 0xffff0000, v96
	v_pk_fma_f32 v[102:103], v[102:103], v[102:103], v[106:107]
	v_lshlrev_b32_e32 v106, 16, v92
	v_and_b32_e32 v107, 0xffff0000, v92
	v_pk_add_f32 v[116:117], v[118:119], v[116:117]
; __device__ __forceinline__ void phase_final(const bf16_t* XA, const bf16_t* Y, const int* tok_info, const float* g, float* out, int wid, int lane) {
;     ...
;             v[j] = xv; ss += (xv[0] * xv[0] + xv[1] * xv[1]) + (xv[2] * xv[2] + xv[3] * xv[3]); }
;         const float r = 1.0f / sqrtf(wave_sum(ss) * (1.0f / 2048.0f) + RMS_EPS);
; #pragma unroll
;         for (int j = 0; j < 8; ++j) { const int o = 4 * lane + 256 * j; *(f32x4*)(out + (size_t)t * D + o) = v[j] * r * gg[j]; xr[j] = nx[j]; ya[j] = na[j]; yb[j] = nb[j]; }
;         e1 = f1; e2 = f2;
;     }
	v_lshlrev_b32_e32 v100, 16, v101
	v_and_b32_e32 v101, 0xffff0000, v101
	v_lshlrev_b32_e32 v96, 16, v97
	v_and_b32_e32 v97, 0xffff0000, v97
	v_pk_add_f32 v[106:107], v[116:117], v[106:107]
	v_lshlrev_b32_e32 v92, 16, v93
	v_and_b32_e32 v93, 0xffff0000, v93
	v_pk_add_f32 v[96:97], v[96:97], v[100:101]
	v_lshlrev_b32_e32 v118, 16, v78
	v_and_b32_e32 v119, 0xffff0000, v78
	v_lshlrev_b32_e32 v130, 16, v52
	v_and_b32_e32 v131, 0xffff0000, v52
	v_lshlrev_b32_e32 v78, 16, v79
	v_and_b32_e32 v79, 0xffff0000, v79
	v_lshlrev_b32_e32 v52, 16, v53
	v_and_b32_e32 v53, 0xffff0000, v53
	v_pk_add_f32 v[92:93], v[96:97], v[92:93]
	v_mul_f32_e32 v2, v107, v107
	v_lshlrev_b32_e32 v116, 16, v66
	v_and_b32_e32 v117, 0xffff0000, v66
	v_pk_add_f32 v[118:119], v[130:131], v[118:119]
	v_lshlrev_b32_e32 v66, 16, v67
	v_and_b32_e32 v67, 0xffff0000, v67
	v_pk_add_f32 v[52:53], v[52:53], v[78:79]
	v_pk_fma_f32 v[96:97], v[106:107], v[106:107], v[2:3] op_sel_hi:[1,1,0]
	v_mul_f32_e32 v2, v93, v93
	v_pk_add_f32 v[116:117], v[118:119], v[116:117]
	v_pk_add_f32 v[52:53], v[52:53], v[66:67]
	v_pk_add_f32 v[110:111], v[110:111], v[110:111] op_sel:[0,1] op_sel_hi:[1,0]
	v_pk_add_f32 v[102:103], v[102:103], v[102:103] op_sel:[0,1] op_sel_hi:[1,0]
	v_pk_fma_f32 v[100:101], v[92:93], v[92:93], v[2:3] op_sel_hi:[1,1,0]
	v_pk_mul_f32 v[66:67], v[116:117], v[116:117]
	v_pk_mul_f32 v[78:79], v[52:53], v[52:53]
	v_mov_b32_e32 v111, v66
	v_mov_b32_e32 v103, v67
	v_mov_b32_e32 v97, v78
	v_mov_b32_e32 v101, v79
	v_pk_add_f32 v[66:67], v[110:111], v[102:103]
	v_pk_add_f32 v[78:79], v[96:97], v[100:101]
	s_cmpk_lt_i32 s4, 0x4000
	v_pk_add_f32 v[66:67], v[66:67], v[78:79]
	s_waitcnt vmcnt(3)
	v_mov_b64_e32 v[110:111], v[88:89]
	v_add_f32_e32 v2, v66, v67
	s_waitcnt lgkmcnt(0)
	s_nop 1
	v_add_f32_dpp v2, v2, v2 quad_perm:[1,0,3,2] row_mask:0xf bank_mask:0xf
	s_nop 1
	v_add_f32_dpp v2, v2, v2 quad_perm:[2,3,0,1] row_mask:0xf bank_mask:0xf
	s_nop 1
	v_add_f32_dpp v2, v2, v2 row_half_mirror row_mask:0xf bank_mask:0xf
	s_nop 1
	v_add_f32_dpp v2, v2, v2 row_mirror row_mask:0xf bank_mask:0xf
	v_mov_b32_e32 v66, v2
	s_nop 1
	v_permlane16_swap_b32_e32 v66, v2
	v_add_f32_e32 v2, v2, v66
	v_mov_b32_e32 v66, v2
	s_nop 1
	v_permlane32_swap_b32_e32 v66, v2
	v_add_f32_e32 v2, v2, v66
	v_mov_b64_e32 v[136:137], v[58:59]
	v_mov_b64_e32 v[130:131], v[60:61]
	v_mov_b64_e32 v[118:119], v[62:63]
	v_fmamk_f32 v2, v2, 0x3a000000, v191
	v_mul_f32_e32 v66, 0x4f800000, v2
	v_cmp_gt_f32_e32 vcc, s39, v2
	s_nop 1
	v_cndmask_b32_e32 v2, v2, v66, vcc
	v_sqrt_f32_e32 v66, v2
	s_nop 0
	v_add_u32_e32 v67, -1, v66
	v_fma_f32 v78, -v67, v66, v2
	v_cmp_ge_f32_e64 s[2:3], 0, v78
	v_add_u32_e32 v78, 1, v66
	s_nop 0
	v_cndmask_b32_e64 v67, v66, v67, s[2:3]
	v_fma_f32 v66, -v78, v66, v2
	v_cmp_lt_f32_e64 s[2:3], 0, v66
	s_nop 1
	v_cndmask_b32_e64 v66, v67, v78, s[2:3]
	v_mul_f32_e32 v67, 0x37800000, v66
	v_cndmask_b32_e32 v66, v66, v67, vcc
	v_cmp_class_f32_e32 vcc, v2, v201
	s_nop 1
	v_cndmask_b32_e32 v2, v66, v2, vcc
	v_div_scale_f32 v66, s[2:3], v2, v2, 1.0
	v_rcp_f32_e32 v67, v66
	v_readlane_b32 s2, v254, 35
	v_readlane_b32 s3, v254, 36
	v_fma_f32 v78, -v66, v67, 1.0
	v_fmac_f32_e32 v67, v78, v67
	v_div_scale_f32 v78, vcc, 1.0, v2, 1.0
	v_mul_f32_e32 v79, v78, v67
	v_fma_f32 v96, -v66, v79, v78
	v_fmac_f32_e32 v79, v96, v67
	v_fma_f32 v66, -v66, v79, v78
	v_div_fmas_f32 v66, v66, v67, v79
	v_div_fixup_f32 v2, v66, v2, 1.0
	v_pk_mul_f32 v[66:67], v[120:121], v[2:3] op_sel_hi:[1,0]
	v_pk_mul_f32 v[78:79], v[124:125], v[2:3] op_sel_hi:[1,0]
	v_pk_mul_f32 v[100:101], v[4:5], v[66:67]
	v_pk_mul_f32 v[102:103], v[6:7], v[78:79]
	v_pk_mul_f32 v[66:67], v[126:127], v[2:3] op_sel_hi:[1,0]
	v_pk_mul_f32 v[78:79], v[132:133], v[2:3] op_sel_hi:[1,0]
	global_store_dwordx4 v[40:41], v[100:103], off offset:-4096
	v_pk_mul_f32 v[52:53], v[52:53], v[2:3] op_sel_hi:[1,0]
	s_waitcnt vmcnt(2)
	v_mov_b64_e32 v[96:97], v[94:95]
	v_pk_mul_f32 v[102:103], v[10:11], v[78:79]
	v_pk_mul_f32 v[100:101], v[8:9], v[66:67]
	v_pk_mul_f32 v[66:67], v[134:135], v[2:3] op_sel_hi:[1,0]
	v_pk_mul_f32 v[78:79], v[122:123], v[2:3] op_sel_hi:[1,0]
	global_store_dwordx4 v[40:41], v[100:103], off offset:-3072
	v_mov_b64_e32 v[134:135], v[72:73]
	v_mov_b64_e32 v[126:127], v[70:71]
	v_pk_mul_f32 v[102:103], v[14:15], v[78:79]
	v_pk_mul_f32 v[100:101], v[12:13], v[66:67]
	v_pk_mul_f32 v[66:67], v[128:129], v[2:3] op_sel_hi:[1,0]
	v_pk_mul_f32 v[78:79], v[114:115], v[2:3] op_sel_hi:[1,0]
	global_store_dwordx4 v[40:41], v[100:103], off offset:-2048
	v_mov_b64_e32 v[128:129], v[74:75]
	v_mov_b64_e32 v[124:125], v[42:43]
	v_pk_mul_f32 v[102:103], v[18:19], v[78:79]
	v_pk_mul_f32 v[100:101], v[16:17], v[66:67]
	v_pk_mul_f32 v[66:67], v[138:139], v[2:3] op_sel_hi:[1,0]
	v_pk_mul_f32 v[78:79], v[108:109], v[2:3] op_sel_hi:[1,0]
	global_store_dwordx4 v[40:41], v[100:103], off offset:-1024
	v_mov_b64_e32 v[138:139], v[56:57]
	v_mov_b64_e32 v[132:133], v[44:45]
	v_pk_mul_f32 v[102:103], v[22:23], v[78:79]
	v_pk_mul_f32 v[100:101], v[20:21], v[66:67]
	v_pk_mul_f32 v[66:67], v[112:113], v[2:3] op_sel_hi:[1,0]
	v_pk_mul_f32 v[78:79], v[104:105], v[2:3] op_sel_hi:[1,0]
	global_store_dwordx4 v[40:41], v[100:103], off
	v_mov_b64_e32 v[104:105], v[90:91]
	v_mov_b64_e32 v[112:113], v[80:81]
	v_pk_mul_f32 v[102:103], v[26:27], v[78:79]
	v_pk_mul_f32 v[100:101], v[24:25], v[66:67]
	v_pk_mul_f32 v[66:67], v[106:107], v[2:3] op_sel_hi:[1,0]
	v_pk_mul_f32 v[78:79], v[92:93], v[2:3] op_sel_hi:[1,0]
	global_store_dwordx4 v[40:41], v[100:103], off offset:1024
	v_mov_b64_e32 v[106:107], v[82:83]
	v_mov_b64_e32 v[122:123], v[46:47]
	v_pk_mul_f32 v[102:103], v[30:31], v[78:79]
	v_pk_mul_f32 v[100:101], v[28:29], v[66:67]
	v_pk_mul_f32 v[66:67], v[116:117], v[2:3] op_sel_hi:[1,0]
	global_store_dwordx4 v[40:41], v[100:103], off offset:2048
	v_mov_b64_e32 v[116:117], v[76:77]
	v_mov_b64_e32 v[78:79], v[86:87]
	v_pk_mul_f32 v[102:103], v[34:35], v[52:53]
	v_pk_mul_f32 v[100:101], v[32:33], v[66:67]
	global_store_dwordx4 v[40:41], v[100:103], off offset:3072
	v_lshl_add_u64 v[40:41], v[40:41], 0, s[2:3]
	s_waitcnt vmcnt(8)
	v_mov_b64_e32 v[52:53], v[98:99]
	v_mov_b64_e32 v[100:101], v[84:85]
	v_mov_b64_e32 v[114:115], v[48:49]
	v_mov_b64_e32 v[108:109], v[50:51]
	v_mov_b64_e32 v[102:103], v[54:55]
	v_mov_b64_e32 v[92:93], v[64:65]
	v_mov_b64_e32 v[66:67], v[68:69]
	s_cbranch_scc0 .LBB0_2986
